# attention: next step's first QK MFMA issued directly behind the loop-back barrier (ahead of pointer advance and back edge)
# baseline (speedup 1.0000x reference)
.LBB0_1629:
	s_or_b64 exec, exec, s[2:3]
	s_mov_b32 s2, 0x40000
	s_nop 1
	v_exp_f32_e32 v174, v4
	v_exp_f32_e32 v176, v5
	s_nop 0
	v_and_b32_e32 v152, 63, v150
	v_lshlrev_b32_e32 v5, 4, v152
	v_exp_f32_e32 v178, v6
	v_lshlrev_b32_e32 v4, 3, v152
	v_and_b32_e32 v5, 0xc0, v5
	v_lshlrev_b32_e32 v6, 1, v152
	v_and_or_b32 v5, v4, 24, v5
	v_and_b32_e32 v6, 32, v6
	v_and_b32_e32 v4, 0x100, v4
	v_or3_b32 v155, v5, v6, v4
	v_bitop3_b32 v4, v151, v150, 15 bitop3:0x78
	s_waitcnt lgkmcnt(0)
	s_barrier
	v_and_b32_e32 v6, 15, v150
	v_lshl_add_u32 v4, v4, 4, v164
	ds_read_b128 v[52:55], v4 offset:16384
	ds_read_b128 v[56:59], v4 offset:24576
	v_bitop3_b32 v4, v151, v6, 2 bitop3:0x36
	v_lshl_add_u32 v4, v4, 4, v164
	ds_read_b128 v[132:135], v4 offset:16384
	ds_read_b128 v[124:127], v4 offset:24576
	v_bitop3_b32 v4, v151, v6, 4 bitop3:0x36
	v_and_b32_e32 v6, 7, v6
	v_lshl_add_u32 v4, v4, 4, v164
	ds_read_b128 v[128:131], v4 offset:16384
	ds_read_b128 v[120:123], v4 offset:24576
	s_lshl_b64 s[20:21], s[36:37], 23
	v_lshlrev_b64 v[4:5], 11, v[28:29]
	v_exp_f32_e32 v180, v7
	v_exp_f32_e32 v182, v8
	v_exp_f32_e32 v184, v9
	v_exp_f32_e32 v186, v10
	v_exp_f32_e32 v187, v11
	v_exp_f32_e32 v175, v12
	v_exp_f32_e32 v177, v13
	v_exp_f32_e32 v179, v14
	v_exp_f32_e32 v181, v15
	v_exp_f32_e32 v183, v16
	v_exp_f32_e32 v185, v17
	v_exp_f32_e32 v188, v18
	v_exp_f32_e32 v189, v19
	v_lshl_add_u64 v[4:5], s[20:21], 0, v[4:5]
	v_lshl_or_b32 v4, v6, 4, v4
	v_lshl_add_u64 v[4:5], v[24:25], 1, v[4:5]
	v_mov_b32_e32 v173, 0
	s_mov_b32 s2, 1
	s_mov_b32 s34, 0
	s_mov_b32 s40, 2
	v_add_u32_e32 v172, 0, v155
	v_mul_hi_u32_u24_e32 v141, 0x2c0, v26
	v_mul_u32_u24_e32 v140, 0x2c0, v26
	v_mul_hi_u32_u24_e32 v143, 0x280, v26
	v_mul_u32_u24_e32 v142, 0x280, v26
	v_mul_hi_u32_u24_e32 v145, 0x240, v26
	v_mul_u32_u24_e32 v144, 0x240, v26
	v_lshlrev_b32_e32 v146, 9, v26
	v_mov_b32_e32 v147, v3
	v_lshl_add_u64 v[148:149], s[14:15], 0, v[4:5]
	s_mov_b32 s3, 0
	s_mov_b32 s41, 1
	s_mov_b32 s43, 2
	s_mov_b32 s42, 1
	v_mov_b32_e32 v4, 0
	v_mov_b32_e32 v5, v173
	v_mov_b32_e32 v6, v173
	v_mov_b32_e32 v7, v173
	v_mov_b32_e32 v8, v173
	v_mov_b32_e32 v9, v173
	v_mov_b32_e32 v10, v173
	v_mov_b32_e32 v11, v173
	v_mov_b32_e32 v12, v173
	v_mov_b32_e32 v13, v173
	v_mov_b32_e32 v14, v173
	v_mov_b32_e32 v15, v173
	v_mov_b32_e32 v16, v173
	v_mov_b32_e32 v17, v173
	v_mov_b32_e32 v18, v173
	v_mov_b32_e32 v19, v173
	v_mov_b32_e32 v20, 0
	v_mov_b32_e32 v21, v173
	v_mov_b32_e32 v22, v173
	v_mov_b32_e32 v23, v173
	v_mov_b32_e32 v24, v173
	v_mov_b32_e32 v25, v173
	v_mov_b32_e32 v26, v173
	v_mov_b32_e32 v27, v173
	v_mov_b32_e32 v28, v173
	v_mov_b32_e32 v29, v173
	v_mov_b32_e32 v30, v173
	v_mov_b32_e32 v31, v173
	v_mov_b32_e32 v32, v173
	v_mov_b32_e32 v33, v173
	v_mov_b32_e32 v34, v173
	v_mov_b32_e32 v35, v173
	s_waitcnt lgkmcnt(0)
	v_mfma_f32_32x32x16_bf16 v[68:83], v[52:55], v[100:103], 0

.LBB0_1640:
	v_add_f32_e32 v36, v191, v36
	v_add_f32_e32 v173, v173, v36
	s_add_i32 s42, s42, 2
	v_add_u32_e32 v36, v174, v168
	ds_read_b128 v[192:195], v36
	v_add_f32_e32 v37, v175, v176
	v_add_f32_e32 v37, v178, v37
	v_add_f32_e32 v37, v180, v37
	v_lshl_add_u32 v212, s19, 13, v172
	s_waitcnt lgkmcnt(7)
	v_exp_f32_e32 v204, v52
	v_exp_f32_e32 v205, v53
	ds_read_b128 v[196:199], v36 offset:8192
	v_add_f32_e32 v36, v183, v37
	v_add_f32_e32 v36, v184, v36
	v_add_f32_e32 v52, v186, v36
	s_waitcnt lgkmcnt(7)
	v_mfma_f32_32x32x16_bf16 v[36:51], v[48:51], v[100:103], 0
	v_exp_f32_e32 v206, v54
	v_exp_f32_e32 v207, v55
	v_add_f32_e32 v191, v187, v52
	v_add_u32_e32 v200, v174, v169
	ds_read_b128 v[52:55], v200
	s_waitcnt lgkmcnt(7)
	v_mfma_f32_32x32x16_bf16 v[68:83], v[132:135], v[96:99], v[68:83]
	v_add_f32_e32 v132, v177, v191
	v_add_f32_e32 v132, v179, v132
	v_add_f32_e32 v132, v181, v132
	v_add_f32_e32 v191, v182, v132
	v_exp_f32_e32 v208, v56
	v_exp_f32_e32 v209, v57
	s_waitcnt lgkmcnt(6)
	v_mfma_f32_32x32x16_bf16 v[36:51], v[120:123], v[96:99], v[36:51]
	ds_read_b128 v[132:135], v200 offset:8192
	v_add_f32_e32 v56, v185, v191
	v_add_f32_e32 v56, v188, v56
	v_add_f32_e32 v56, v189, v56
	v_exp_f32_e32 v210, v58
	v_exp_f32_e32 v211, v59
	v_add_f32_e32 v213, v190, v56
	v_add_u32_e32 v174, v174, v170
	ds_read_b128 v[56:59], v174
	v_cvt_pk_bf16_f32 v120, v175, v176
	v_exp_f32_e32 v175, v60
	v_exp_f32_e32 v176, v61
	s_waitcnt lgkmcnt(7)
	v_mfma_f32_32x32x16_bf16 v[68:83], v[128:131], v[104:107], v[68:83]
	v_cvt_pk_bf16_f32 v121, v178, v180
	v_cvt_pk_bf16_f32 v122, v183, v184
	v_cvt_pk_bf16_f32 v123, v186, v187
	s_waitcnt lgkmcnt(6)
	v_mfma_f32_32x32x16_bf16 v[36:51], v[124:127], v[104:107], v[36:51]
	ds_read_b128 v[200:203], v174 offset:8192
	v_cvt_pk_bf16_f32 v128, v177, v179
	v_exp_f32_e32 v174, v62
	v_exp_f32_e32 v177, v63
	v_cvt_pk_bf16_f32 v129, v181, v182
	v_cvt_pk_bf16_f32 v130, v185, v188
	v_cvt_pk_bf16_f32 v131, v189, v190
	v_exp_f32_e32 v178, v64
	v_exp_f32_e32 v179, v65
	v_permlane32_swap_b32_e32 v120, v122
	v_permlane32_swap_b32_e32 v121, v123
	v_permlane32_swap_b32_e32 v128, v130
	v_permlane32_swap_b32_e32 v129, v131
	s_waitcnt lgkmcnt(5)
	v_mfma_f32_32x32x16_bf16 v[68:83], v[192:195], v[92:95], v[68:83]
	s_waitcnt lgkmcnt(4)
	v_mfma_f32_32x32x16_bf16 v[36:51], v[196:199], v[92:95], v[36:51]
	v_exp_f32_e32 v180, v66
	v_exp_f32_e32 v181, v67
	v_cvt_pk_bf16_f32 v60, v204, v205
	v_cvt_pk_bf16_f32 v61, v206, v207
	v_cvt_pk_bf16_f32 v62, v208, v209
	v_cvt_pk_bf16_f32 v63, v210, v211
	ds_read_b64_tr_b16 v[124:125], v212 offset:49152
	ds_read_b64_tr_b16 v[126:127], v212 offset:50176
	ds_read_b64_tr_b16 v[182:183], v212 offset:49664
	ds_read_b64_tr_b16 v[184:185], v212 offset:50688
	s_waitcnt lgkmcnt(7)
	v_mfma_f32_32x32x16_bf16 v[68:83], v[52:55], v[88:91], v[68:83]
	v_cvt_pk_bf16_f32 v64, v175, v176
	v_cvt_pk_bf16_f32 v65, v174, v177
	v_cvt_pk_bf16_f32 v66, v178, v179
	v_cvt_pk_bf16_f32 v67, v180, v181
	v_permlane32_swap_b32_e32 v60, v62
	v_permlane32_swap_b32_e32 v61, v63
	s_waitcnt lgkmcnt(6)
	v_mfma_f32_32x32x16_bf16 v[36:51], v[132:135], v[88:91], v[36:51]
	ds_read_b64_tr_b16 v[186:187], v212 offset:51200
	ds_read_b64_tr_b16 v[188:189], v212 offset:52224
	ds_read_b64_tr_b16 v[192:193], v212 offset:52736
	ds_read_b64_tr_b16 v[190:191], v212 offset:51712
	v_add_f32_e32 v52, v204, v213
	v_add_f32_e32 v52, v205, v52
	v_add_f32_e32 v52, v206, v52
	v_add_f32_e32 v52, v207, v52
	v_permlane32_swap_b32_e32 v64, v66
	v_permlane32_swap_b32_e32 v65, v67
	ds_read_b64_tr_b16 v[194:195], v212 offset:53248
	ds_read_b64_tr_b16 v[196:197], v212 offset:54272
	ds_read_b64_tr_b16 v[204:205], v212 offset:53760
	ds_read_b64_tr_b16 v[206:207], v212 offset:54784
	v_add_f32_e32 v52, v208, v52
	v_add_f32_e32 v52, v209, v52
	v_add_f32_e32 v52, v210, v52
	v_add_f32_e32 v52, v211, v52
	v_add_f32_e32 v52, v175, v52
	v_add_f32_e32 v52, v176, v52
	s_waitcnt lgkmcnt(13)
	v_mfma_f32_32x32x16_bf16 v[68:83], v[56:59], v[84:87], v[68:83]
	s_waitcnt lgkmcnt(12)
	v_mfma_f32_32x32x16_bf16 v[36:51], v[200:203], v[84:87], v[36:51]
	ds_read_b64_tr_b16 v[208:209], v212 offset:55296
	ds_read_b64_tr_b16 v[210:211], v212 offset:56320
	ds_read_b64_tr_b16 v[220:221], v212 offset:56832
	ds_read_b64_tr_b16 v[218:219], v212 offset:55808
	v_add_f32_e32 v52, v174, v52
	v_add_f32_e32 v52, v177, v52
	v_add_f32_e32 v52, v178, v52
	v_add_f32_e32 v52, v179, v52
	v_add_f32_e32 v52, v180, v52
	v_add_f32_e32 v198, v181, v52
	s_waitcnt lgkmcnt(14)
	v_mfma_f32_32x32x16_bf16 v[4:19], v[120:123], v[124:127], v[4:19]
	v_lshl_add_u32 v179, s34, 14, v164
	v_add_u32_e32 v56, v179, v165
	ds_read_b128 v[52:55], v56
	v_exp_f32_e32 v174, v68
	v_exp_f32_e32 v176, v69
	s_waitcnt lgkmcnt(13)
	v_mfma_f32_32x32x16_bf16 v[20:35], v[120:123], v[182:185], v[20:35]
	ds_read_b128 v[56:59], v56 offset:8192
	v_exp_f32_e32 v178, v70
	v_exp_f32_e32 v180, v71
	s_waitcnt lgkmcnt(12)
	v_mfma_f32_32x32x16_bf16 v[4:19], v[128:131], v[186:189], v[4:19]
	v_add_u32_e32 v68, v179, v166
	ds_read_b128 v[132:135], v68
	v_exp_f32_e32 v182, v72
	v_exp_f32_e32 v184, v73
	s_waitcnt lgkmcnt(11)
	v_mfma_f32_32x32x16_bf16 v[20:35], v[128:131], v[190:193], v[20:35]
	ds_read_b128 v[124:127], v68 offset:8192
	v_exp_f32_e32 v186, v74
	v_exp_f32_e32 v187, v75
	s_waitcnt lgkmcnt(10)
	v_mfma_f32_32x32x16_bf16 v[4:19], v[60:63], v[194:197], v[4:19]
	v_add_u32_e32 v68, v179, v167
	ds_read_b128 v[128:131], v68
	v_exp_f32_e32 v175, v76
	v_exp_f32_e32 v177, v77
	s_waitcnt lgkmcnt(9)
	v_mfma_f32_32x32x16_bf16 v[20:35], v[60:63], v[204:207], v[20:35]
	ds_read_b128 v[120:123], v68 offset:8192
	v_exp_f32_e32 v179, v78
	v_exp_f32_e32 v181, v79
	s_waitcnt lgkmcnt(8)
	v_mfma_f32_32x32x16_bf16 v[4:19], v[64:67], v[208:211], v[4:19]
	v_exp_f32_e32 v183, v80
	v_exp_f32_e32 v185, v81
	s_waitcnt lgkmcnt(6)
	v_mfma_f32_32x32x16_bf16 v[20:35], v[64:67], v[218:221], v[20:35]
	v_exp_f32_e32 v188, v82
	v_exp_f32_e32 v189, v83
	v_mov_b32_e32 v60, v198
	s_nop 1
	v_permlane32_swap_b32_e32 v198, v60
	v_add_f32_e32 v60, v198, v60
	v_add_f32_e32 v173, v173, v60
	s_waitcnt lgkmcnt(0)
	s_barrier
	v_mfma_f32_32x32x16_bf16 v[68:83], v[52:55], v[100:103], 0
	v_lshl_add_u64 v[138:139], v[138:139], 0, v[2:3]
	v_lshl_add_u64 v[148:149], v[148:149], 0, s[74:75]
	s_and_b64 vcc, exec, s[2:3]
	s_cbranch_vccnz .LBB0_1642
	s_mov_b32 s2, s34
	s_mov_b32 s34, s20
	s_mov_b32 s3, s43
	s_mov_b32 s43, s19
	s_branch .LBB0_1630
